# v24: v23 + conversion tickets spread over the whole NSA queue (5 of 12 slots); the dynamic GLA-C units absorb the coarser queue tail
# baseline (speedup 1.0000x reference)
.LBB0_707:
	s_or_b64 exec, exec, s[2:3]
	v_readlane_b32 s6, v254, 60
	s_cmpk_lg_i32 s6, 0x2d8
	s_cbranch_scc1 .Lq_odd
	s_mul_i32 s98, s10, 0x1556
	s_lshr_b32 s98, s98, 16
	s_mul_i32 s99, s98, 12
	s_sub_i32 s99, s10, s99
	s_movk_i32 s101, 0x52a
	s_bfm_b32 s18, s99, 0
	s_and_b32 s18, s18, s101
	s_bcnt1_i32_b32 s18, s18
	s_mul_i32 s98, s98, 5
	s_add_i32 s18, s18, s98
	s_bitcmp1_b32 s101, s99
	s_cselect_b64 s[2:3], -1, 0
	s_branch .Lq_dec
.Lq_odd:
	s_bitcmp1_b32 s10, 0
	s_cselect_b64 s[2:3], -1, 0
	s_ashr_i32 s18, s10, 1
.Lq_dec:
	s_cmp_lt_i32 s18, s6
	s_cselect_b64 s[6:7], -1, 0
	s_and_b64 s[2:3], s[2:3], s[6:7]
	s_andn2_b64 vcc, exec, s[2:3]
	s_mov_b64 s[2:3], -1
	s_cbranch_vccnz .LBB0_710
	s_and_b64 vcc, exec, s[2:3]
	s_cbranch_vccnz .LBB0_938
